# speedup vs baseline: 1.0067x; 1.0005x over previous
.Lnoprio:
	s_waitcnt vmcnt(8)
	v_cmp_ne_u32_e64 s[20:21], 0, v224
	s_add_u32 s31, s23, 1
	s_and_b32 s31, s31, 31
	s_lshl_b32 s31, s31, 8
	s_add_u32 s26, s31, s22
	s_add_u32 s31, s23, 3
	s_and_b32 s31, s31, 31
	s_mul_i32 s31, s31, 0xc0000
	s_add_u32 s24, s31, s18
	s_add_u32 s31, s23, 2
	s_and_b32 s31, s31, 31
	s_mul_i32 s31, s31, 0xc0000
	s_add_u32 s25, s31, s19
	s_cmp_eq_u64 s[20:21], -1
	s_cselect_b32 s34, s37, s38
	ds_read_b128 v[176:179], v225 offset:9216
	s_add_u32 s31, s29, 0xc00000
	buffer_load_dwordx4 v[32:35], v243, s[4:7], s31 offen nt
	s_add_u32 s31, s29, 0xc0c000
	buffer_load_dwordx4 v[36:39], v243, s[4:7], s31 offen nt
	buffer_load_dword v224, v230, s[8:11], s26 offen
	v_exp_f32_e32 v64, v64
	v_exp_f32_e32 v65, v65
	v_cvt_pk_f16_f32 v208, v208, v209
	v_cvt_pk_f16_f32 v209, v210, v211
	ds_read_b128 v[180:183], v225 offset:9248
	v_cvt_pk_f16_f32 v160, v64, v65
	v_add_f32_e32 v64, v64, v65
	v_cvt_pk_f16_f32 v212, v212, v213
	v_exp_f32_e32 v66, v66
	v_exp_f32_e32 v67, v67
	v_cvt_pk_f16_f32 v213, v214, v215
	ds_write_b64 v227, v[208:209] offset:18432
	ds_write_b64 v227, v[212:213] offset:23040
	ds_read_b128 v[184:187], v225 offset:9280
	v_cvt_pk_f16_f32 v161, v66, v67
	v_add_f32_e32 v66, v66, v67
	v_exp_f32_e32 v68, v68
	v_exp_f32_e32 v69, v69
	ds_read_b128 v[188:191], v225 offset:9312
	buffer_load_dwordx4 v[208:211], v229, s[4:7], s24 offen
	v_cvt_pk_f16_f32 v162, v68, v69
	v_add_f32_e32 v68, v68, v69
	v_add_f32_e32 v231, v64, v66
	v_exp_f32_e32 v70, v70
	v_exp_f32_e32 v71, v71
	ds_read_b128 v[192:195], v226 offset:0
	buffer_load_dwordx4 v[212:215], v252, s[4:7], s24 offen
	v_cvt_pk_f16_f32 v163, v70, v71
	v_add_f32_e32 v70, v70, v71
	v_add_f32_e32 v231, v231, v68
	v_exp_f32_e32 v72, v72
	v_exp_f32_e32 v73, v73
	ds_read_b128 v[196:199], v226 offset:4608
	v_cvt_pk_f16_f32 v164, v72, v73
	v_add_f32_e32 v72, v72, v73
	v_add_f32_e32 v231, v231, v70
	v_exp_f32_e32 v74, v74
	v_exp_f32_e32 v75, v75
	ds_read_b128 v[200:203], v226 offset:32
	v_cvt_pk_f16_f32 v165, v74, v75
	v_add_f32_e32 v74, v74, v75
	v_add_f32_e32 v231, v231, v72
	v_exp_f32_e32 v76, v76
	v_exp_f32_e32 v77, v77
	ds_read_b128 v[204:207], v226 offset:4640
	v_cvt_pk_f16_f32 v166, v76, v77
	v_add_f32_e32 v76, v76, v77
	v_add_f32_e32 v231, v231, v74
	v_exp_f32_e32 v78, v78
	v_exp_f32_e32 v79, v79
	v_add_f32_e32 v231, v231, v76
	v_cvt_pk_f16_f32 v167, v78, v79
	v_add_f32_e32 v78, v78, v79
	v_add_f32_e32 v231, v231, v78
	v_cmp_nge_f32_e32 vcc, s34, v231
	s_cbranch_vccnz .Lovf_a1_00
.Lovfret_a1_00:
	v_add_f32_e32 v232, v232, v231
	s_waitcnt lgkmcnt(4)
	v_mfma_f32_32x32x16_f16 v[64:79], v[176:179], v[128:131], v[96:111]
	ds_read_b128 v[176:179], v225 offset:13824
	s_waitcnt vmcnt(5)
	v_exp_f32_e32 v80, v80
	v_exp_f32_e32 v81, v81
	v_cvt_pk_f16_f32 v216, v216, v217
	v_cvt_pk_f16_f32 v217, v218, v219
	v_mfma_f32_32x32x16_f16 v[64:79], v[180:183], v[132:135], v[64:79]
	ds_read_b128 v[180:183], v225 offset:13856
	v_cvt_pk_f16_f32 v168, v80, v81
	v_add_f32_e32 v80, v80, v81
	v_cvt_pk_f16_f32 v218, v220, v221
	v_exp_f32_e32 v82, v82
	v_exp_f32_e32 v83, v83
	v_cvt_pk_f16_f32 v219, v222, v223
	v_mfma_f32_32x32x16_f16 v[64:79], v[184:187], v[136:139], v[64:79]
	ds_write_b128 v228, v[216:219] offset:9216
	ds_read_b128 v[184:187], v225 offset:13888
	v_cvt_pk_f16_f32 v169, v82, v83
	v_add_f32_e32 v82, v82, v83
	v_exp_f32_e32 v84, v84
	v_exp_f32_e32 v85, v85
	v_mfma_f32_32x32x16_f16 v[64:79], v[188:191], v[140:143], v[64:79]
	ds_read_b128 v[188:191], v225 offset:13920
	buffer_load_dword v216, v230, s[4:7], s25 offen
	buffer_load_dword v217, v245, s[4:7], s25 offen
	v_cvt_pk_f16_f32 v170, v84, v85
	v_add_f32_e32 v84, v84, v85
	v_add_f32_e32 v231, v80, v82
	v_exp_f32_e32 v86, v86
	v_exp_f32_e32 v87, v87
	s_waitcnt lgkmcnt(5)
	v_mfma_f32_32x32x16_f16 v[0:15], v[192:195], v[160:163], v[0:15]
	ds_read_b128 v[192:195], v226 offset:64
	buffer_load_dword v218, v246, s[4:7], s25 offen
	buffer_load_dword v219, v247, s[4:7], s25 offen
	v_cvt_pk_f16_f32 v171, v86, v87
	v_add_f32_e32 v86, v86, v87
	v_add_f32_e32 v231, v231, v84
	v_exp_f32_e32 v88, v88
	v_exp_f32_e32 v89, v89
	v_mfma_f32_32x32x16_f16 v[16:31], v[196:199], v[160:163], v[16:31]
	ds_read_b128 v[196:199], v226 offset:4672
	buffer_load_dword v220, v248, s[4:7], s25 offen
	buffer_load_dword v221, v249, s[4:7], s25 offen
	v_cvt_pk_f16_f32 v172, v88, v89
	v_add_f32_e32 v88, v88, v89
	v_add_f32_e32 v231, v231, v86
	v_exp_f32_e32 v90, v90
	v_exp_f32_e32 v91, v91
	v_mfma_f32_32x32x16_f16 v[0:15], v[200:203], v[164:167], v[0:15]
	ds_read_b128 v[200:203], v226 offset:96
	buffer_load_dword v222, v250, s[4:7], s25 offen
	v_cvt_pk_f16_f32 v173, v90, v91
	v_add_f32_e32 v90, v90, v91
	v_add_f32_e32 v231, v231, v88
	v_exp_f32_e32 v92, v92
	v_exp_f32_e32 v93, v93
	v_mfma_f32_32x32x16_f16 v[16:31], v[204:207], v[164:167], v[16:31]
	ds_read_b128 v[204:207], v226 offset:4704
	buffer_load_dword v223, v251, s[4:7], s25 offen
	v_cvt_pk_f16_f32 v174, v92, v93
	v_add_f32_e32 v92, v92, v93
	v_add_f32_e32 v231, v231, v90
	v_exp_f32_e32 v94, v94
	v_exp_f32_e32 v95, v95
	v_add_f32_e32 v231, v231, v92
	v_cvt_pk_f16_f32 v175, v94, v95
	v_add_f32_e32 v94, v94, v95
	v_add_f32_e32 v231, v231, v94
	v_cmp_nge_f32_e32 vcc, s34, v231
	s_cbranch_vccnz .Lovf_a1_01
.Lovfret_a1_01:
	v_add_f32_e32 v232, v232, v231
	s_waitcnt lgkmcnt(6)
	s_barrier
	s_add_u32 s23, s23, 1
	s_waitcnt vmcnt(8)
	v_cmp_ne_u32_e64 s[20:21], 0, v224
	s_add_u32 s31, s23, 1
	s_and_b32 s31, s31, 31
	s_lshl_b32 s31, s31, 8
	s_add_u32 s26, s31, s22
	s_add_u32 s31, s23, 3
	s_and_b32 s31, s31, 31
	s_mul_i32 s31, s31, 0xc0000
	s_add_u32 s24, s31, s18
	s_add_u32 s31, s23, 2
	s_and_b32 s31, s31, 31
	s_mul_i32 s31, s31, 0xc0000
	s_add_u32 s25, s31, s19
	s_cmp_eq_u64 s[20:21], -1
	s_cselect_b32 s34, s37, s38
	s_waitcnt lgkmcnt(4)
	v_mfma_f32_32x32x16_f16 v[80:95], v[176:179], v[128:131], v[96:111]
	ds_read_b128 v[176:179], v225 offset:18432
	s_add_u32 s31, s29, 0xc18000
	buffer_load_dwordx4 v[40:43], v243, s[4:7], s31 offen nt
	s_add_u32 s31, s29, 0xc24000
	buffer_load_dwordx4 v[44:47], v243, s[4:7], s31 offen nt
	buffer_load_dword v224, v230, s[8:11], s26 offen
	v_exp_f32_e32 v64, v64
	v_exp_f32_e32 v65, v65
	v_cvt_pk_f16_f32 v208, v208, v209
	v_cvt_pk_f16_f32 v209, v210, v211
	v_mfma_f32_32x32x16_f16 v[80:95], v[180:183], v[132:135], v[80:95]
	ds_read_b128 v[180:183], v225 offset:18464
	v_cvt_pk_f16_f32 v160, v64, v65
	v_add_f32_e32 v64, v64, v65
	v_cvt_pk_f16_f32 v212, v212, v213
	v_exp_f32_e32 v66, v66
	v_exp_f32_e32 v67, v67
	v_cvt_pk_f16_f32 v213, v214, v215
	v_mfma_f32_32x32x16_f16 v[80:95], v[184:187], v[136:139], v[80:95]
	ds_write_b64 v227, v[208:209] offset:27648
	ds_write_b64 v227, v[212:213] offset:32256
	ds_read_b128 v[184:187], v225 offset:18496
	v_cvt_pk_f16_f32 v161, v66, v67
	v_add_f32_e32 v66, v66, v67
	v_exp_f32_e32 v68, v68
	v_exp_f32_e32 v69, v69
	v_mfma_f32_32x32x16_f16 v[80:95], v[188:191], v[140:143], v[80:95]
	ds_read_b128 v[188:191], v225 offset:18528
	buffer_load_dwordx4 v[208:211], v229, s[4:7], s24 offen
	v_cvt_pk_f16_f32 v162, v68, v69
	v_add_f32_e32 v68, v68, v69
	v_add_f32_e32 v231, v64, v66
	v_exp_f32_e32 v70, v70
	v_exp_f32_e32 v71, v71
	s_waitcnt lgkmcnt(6)
	v_mfma_f32_32x32x16_f16 v[0:15], v[192:195], v[168:171], v[0:15]
	ds_read_b128 v[192:195], v226 offset:9216
	buffer_load_dwordx4 v[212:215], v252, s[4:7], s24 offen
	v_cvt_pk_f16_f32 v163, v70, v71
	v_add_f32_e32 v70, v70, v71
	v_add_f32_e32 v231, v231, v68
	v_exp_f32_e32 v72, v72
	v_exp_f32_e32 v73, v73
	v_mfma_f32_32x32x16_f16 v[16:31], v[196:199], v[168:171], v[16:31]
	ds_read_b128 v[196:199], v226 offset:13824
	v_cvt_pk_f16_f32 v164, v72, v73
	v_add_f32_e32 v72, v72, v73
	v_add_f32_e32 v231, v231, v70
	v_exp_f32_e32 v74, v74
	v_exp_f32_e32 v75, v75
	v_mfma_f32_32x32x16_f16 v[0:15], v[200:203], v[172:175], v[0:15]
	ds_read_b128 v[200:203], v226 offset:9248
	v_cvt_pk_f16_f32 v165, v74, v75
	v_add_f32_e32 v74, v74, v75
	v_add_f32_e32 v231, v231, v72
	v_exp_f32_e32 v76, v76
	v_exp_f32_e32 v77, v77
	v_mfma_f32_32x32x16_f16 v[16:31], v[204:207], v[172:175], v[16:31]
	ds_read_b128 v[204:207], v226 offset:13856
	v_cvt_pk_f16_f32 v166, v76, v77
	v_add_f32_e32 v76, v76, v77
	v_add_f32_e32 v231, v231, v74
	v_exp_f32_e32 v78, v78
	v_exp_f32_e32 v79, v79
	v_add_f32_e32 v231, v231, v76
	v_cvt_pk_f16_f32 v167, v78, v79
	v_add_f32_e32 v78, v78, v79
	v_add_f32_e32 v231, v231, v78
	v_cmp_nge_f32_e32 vcc, s34, v231
	s_cbranch_vccnz .Lovf_a1_10
.Lovfret_a1_10:
	v_add_f32_e32 v232, v232, v231
	s_waitcnt lgkmcnt(4)
	v_mfma_f32_32x32x16_f16 v[64:79], v[176:179], v[128:131], v[96:111]
	ds_read_b128 v[176:179], v225 offset:23040
	s_waitcnt vmcnt(5)
	v_exp_f32_e32 v80, v80
	v_exp_f32_e32 v81, v81
	v_cvt_pk_f16_f32 v216, v216, v217
	v_cvt_pk_f16_f32 v217, v218, v219
	v_mfma_f32_32x32x16_f16 v[64:79], v[180:183], v[132:135], v[64:79]
	ds_read_b128 v[180:183], v225 offset:23072
	v_cvt_pk_f16_f32 v168, v80, v81
	v_add_f32_e32 v80, v80, v81
	v_cvt_pk_f16_f32 v218, v220, v221
	v_exp_f32_e32 v82, v82
	v_exp_f32_e32 v83, v83
	v_cvt_pk_f16_f32 v219, v222, v223
	v_mfma_f32_32x32x16_f16 v[64:79], v[184:187], v[136:139], v[64:79]
	ds_write_b128 v228, v[216:219] offset:18432
	ds_read_b128 v[184:187], v225 offset:23104
	v_cvt_pk_f16_f32 v169, v82, v83
	v_add_f32_e32 v82, v82, v83
	v_exp_f32_e32 v84, v84
	v_exp_f32_e32 v85, v85
	v_mfma_f32_32x32x16_f16 v[64:79], v[188:191], v[140:143], v[64:79]
	ds_read_b128 v[188:191], v225 offset:23136
	buffer_load_dword v216, v230, s[4:7], s25 offen
	buffer_load_dword v217, v245, s[4:7], s25 offen
	v_cvt_pk_f16_f32 v170, v84, v85
	v_add_f32_e32 v84, v84, v85
	v_add_f32_e32 v231, v80, v82
	v_exp_f32_e32 v86, v86
	v_exp_f32_e32 v87, v87
	s_waitcnt lgkmcnt(5)
	v_mfma_f32_32x32x16_f16 v[0:15], v[192:195], v[160:163], v[0:15]
	ds_read_b128 v[192:195], v226 offset:9280
	buffer_load_dword v218, v246, s[4:7], s25 offen
	buffer_load_dword v219, v247, s[4:7], s25 offen
	v_cvt_pk_f16_f32 v171, v86, v87
	v_add_f32_e32 v86, v86, v87
	v_add_f32_e32 v231, v231, v84
	v_exp_f32_e32 v88, v88
	v_exp_f32_e32 v89, v89
	v_mfma_f32_32x32x16_f16 v[16:31], v[196:199], v[160:163], v[16:31]
	ds_read_b128 v[196:199], v226 offset:13888
	buffer_load_dword v220, v248, s[4:7], s25 offen
	buffer_load_dword v221, v249, s[4:7], s25 offen
	v_cvt_pk_f16_f32 v172, v88, v89
	v_add_f32_e32 v88, v88, v89
	v_add_f32_e32 v231, v231, v86
	v_exp_f32_e32 v90, v90
	v_exp_f32_e32 v91, v91
	v_mfma_f32_32x32x16_f16 v[0:15], v[200:203], v[164:167], v[0:15]
	ds_read_b128 v[200:203], v226 offset:9312
	buffer_load_dword v222, v250, s[4:7], s25 offen
	v_cvt_pk_f16_f32 v173, v90, v91
	v_add_f32_e32 v90, v90, v91
	v_add_f32_e32 v231, v231, v88
	v_exp_f32_e32 v92, v92
	v_exp_f32_e32 v93, v93
	v_mfma_f32_32x32x16_f16 v[16:31], v[204:207], v[164:167], v[16:31]
	ds_read_b128 v[204:207], v226 offset:13920
	buffer_load_dword v223, v251, s[4:7], s25 offen
	v_cvt_pk_f16_f32 v174, v92, v93
	v_add_f32_e32 v92, v92, v93
	v_add_f32_e32 v231, v231, v90
	v_exp_f32_e32 v94, v94
	v_exp_f32_e32 v95, v95
	v_add_f32_e32 v231, v231, v92
	v_cvt_pk_f16_f32 v175, v94, v95
	v_add_f32_e32 v94, v94, v95
	v_add_f32_e32 v231, v231, v94
	v_cmp_nge_f32_e32 vcc, s34, v231
	s_cbranch_vccnz .Lovf_a1_11
.Lovfret_a1_11:
	v_add_f32_e32 v232, v232, v231
	s_waitcnt lgkmcnt(6)
	s_barrier
	s_add_u32 s23, s23, 1
	s_waitcnt vmcnt(8)
	v_cmp_ne_u32_e64 s[20:21], 0, v224
	s_add_u32 s31, s23, 1
	s_and_b32 s31, s31, 31
	s_lshl_b32 s31, s31, 8
	s_add_u32 s26, s31, s22
	s_add_u32 s31, s23, 3
	s_and_b32 s31, s31, 31
	s_mul_i32 s31, s31, 0xc0000
	s_add_u32 s24, s31, s18
	s_add_u32 s31, s23, 2
	s_and_b32 s31, s31, 31
	s_mul_i32 s31, s31, 0xc0000
	s_add_u32 s25, s31, s19
	s_cmp_eq_u64 s[20:21], -1
	s_cselect_b32 s34, s37, s38
	s_waitcnt lgkmcnt(4)
	v_mfma_f32_32x32x16_f16 v[80:95], v[176:179], v[128:131], v[96:111]
	ds_read_b128 v[176:179], v225 offset:27648
	s_add_u32 s31, s29, 0xc30000
	buffer_load_dwordx4 v[48:51], v243, s[4:7], s31 offen nt
	s_add_u32 s31, s29, 0xc3c000
	buffer_load_dwordx4 v[52:55], v243, s[4:7], s31 offen nt
	buffer_load_dword v224, v230, s[8:11], s26 offen
	v_exp_f32_e32 v64, v64
	v_exp_f32_e32 v65, v65
	v_cvt_pk_f16_f32 v208, v208, v209
	v_cvt_pk_f16_f32 v209, v210, v211
	v_mfma_f32_32x32x16_f16 v[80:95], v[180:183], v[132:135], v[80:95]
	ds_read_b128 v[180:183], v225 offset:27680
	v_cvt_pk_f16_f32 v160, v64, v65
	v_add_f32_e32 v64, v64, v65
	v_cvt_pk_f16_f32 v212, v212, v213
	v_exp_f32_e32 v66, v66
	v_exp_f32_e32 v67, v67
	v_cvt_pk_f16_f32 v213, v214, v215
	v_mfma_f32_32x32x16_f16 v[80:95], v[184:187], v[136:139], v[80:95]
	ds_write_b64 v227, v[208:209] offset:0
	ds_write_b64 v227, v[212:213] offset:4608
	ds_read_b128 v[184:187], v225 offset:27712
	v_cvt_pk_f16_f32 v161, v66, v67
	v_add_f32_e32 v66, v66, v67
	v_exp_f32_e32 v68, v68
	v_exp_f32_e32 v69, v69
	v_mfma_f32_32x32x16_f16 v[80:95], v[188:191], v[140:143], v[80:95]
	ds_read_b128 v[188:191], v225 offset:27744
	buffer_load_dwordx4 v[208:211], v229, s[4:7], s24 offen
	v_cvt_pk_f16_f32 v162, v68, v69
	v_add_f32_e32 v68, v68, v69
	v_add_f32_e32 v231, v64, v66
	v_exp_f32_e32 v70, v70
	v_exp_f32_e32 v71, v71
	s_waitcnt lgkmcnt(6)
	v_mfma_f32_32x32x16_f16 v[0:15], v[192:195], v[168:171], v[0:15]
	ds_read_b128 v[192:195], v226 offset:18432
	buffer_load_dwordx4 v[212:215], v252, s[4:7], s24 offen
	v_cvt_pk_f16_f32 v163, v70, v71
	v_add_f32_e32 v70, v70, v71
	v_add_f32_e32 v231, v231, v68
	v_exp_f32_e32 v72, v72
	v_exp_f32_e32 v73, v73
	v_mfma_f32_32x32x16_f16 v[16:31], v[196:199], v[168:171], v[16:31]
	ds_read_b128 v[196:199], v226 offset:23040
	v_cvt_pk_f16_f32 v164, v72, v73
	v_add_f32_e32 v72, v72, v73
	v_add_f32_e32 v231, v231, v70
	v_exp_f32_e32 v74, v74
	v_exp_f32_e32 v75, v75
	v_mfma_f32_32x32x16_f16 v[0:15], v[200:203], v[172:175], v[0:15]
	ds_read_b128 v[200:203], v226 offset:18464
	v_cvt_pk_f16_f32 v165, v74, v75
	v_add_f32_e32 v74, v74, v75
	v_add_f32_e32 v231, v231, v72
	v_exp_f32_e32 v76, v76
	v_exp_f32_e32 v77, v77
	v_mfma_f32_32x32x16_f16 v[16:31], v[204:207], v[172:175], v[16:31]
	ds_read_b128 v[204:207], v226 offset:23072
	v_cvt_pk_f16_f32 v166, v76, v77
	v_add_f32_e32 v76, v76, v77
	v_add_f32_e32 v231, v231, v74
	v_exp_f32_e32 v78, v78
	v_exp_f32_e32 v79, v79
	v_add_f32_e32 v231, v231, v76
	v_cvt_pk_f16_f32 v167, v78, v79
	v_add_f32_e32 v78, v78, v79
	v_add_f32_e32 v231, v231, v78
	v_cmp_nge_f32_e32 vcc, s34, v231
	s_cbranch_vccnz .Lovf_a1_20
.Lovfret_a1_20:
	v_add_f32_e32 v232, v232, v231
	s_waitcnt lgkmcnt(4)
	v_mfma_f32_32x32x16_f16 v[64:79], v[176:179], v[128:131], v[96:111]
	ds_read_b128 v[176:179], v225 offset:32256
	s_waitcnt vmcnt(5)
	v_exp_f32_e32 v80, v80
	v_exp_f32_e32 v81, v81
	v_cvt_pk_f16_f32 v216, v216, v217
	v_cvt_pk_f16_f32 v217, v218, v219
	v_mfma_f32_32x32x16_f16 v[64:79], v[180:183], v[132:135], v[64:79]
	ds_read_b128 v[180:183], v225 offset:32288
	v_cvt_pk_f16_f32 v168, v80, v81
	v_add_f32_e32 v80, v80, v81
	v_cvt_pk_f16_f32 v218, v220, v221
	v_exp_f32_e32 v82, v82
	v_exp_f32_e32 v83, v83
	v_cvt_pk_f16_f32 v219, v222, v223
	v_mfma_f32_32x32x16_f16 v[64:79], v[184:187], v[136:139], v[64:79]
	ds_write_b128 v228, v[216:219] offset:27648
	ds_read_b128 v[184:187], v225 offset:32320
	v_cvt_pk_f16_f32 v169, v82, v83
	v_add_f32_e32 v82, v82, v83
	v_exp_f32_e32 v84, v84
	v_exp_f32_e32 v85, v85
	v_mfma_f32_32x32x16_f16 v[64:79], v[188:191], v[140:143], v[64:79]
	ds_read_b128 v[188:191], v225 offset:32352
	buffer_load_dword v216, v230, s[4:7], s25 offen
	buffer_load_dword v217, v245, s[4:7], s25 offen
	v_cvt_pk_f16_f32 v170, v84, v85
	v_add_f32_e32 v84, v84, v85
	v_add_f32_e32 v231, v80, v82
	v_exp_f32_e32 v86, v86
	v_exp_f32_e32 v87, v87
	s_waitcnt lgkmcnt(5)
	v_mfma_f32_32x32x16_f16 v[0:15], v[192:195], v[160:163], v[0:15]
	ds_read_b128 v[192:195], v226 offset:18496
	buffer_load_dword v218, v246, s[4:7], s25 offen
	buffer_load_dword v219, v247, s[4:7], s25 offen
	v_cvt_pk_f16_f32 v171, v86, v87
	v_add_f32_e32 v86, v86, v87
	v_add_f32_e32 v231, v231, v84
	v_exp_f32_e32 v88, v88
	v_exp_f32_e32 v89, v89
	v_mfma_f32_32x32x16_f16 v[16:31], v[196:199], v[160:163], v[16:31]
	ds_read_b128 v[196:199], v226 offset:23104
	buffer_load_dword v220, v248, s[4:7], s25 offen
	buffer_load_dword v221, v249, s[4:7], s25 offen
	v_cvt_pk_f16_f32 v172, v88, v89
	v_add_f32_e32 v88, v88, v89
	v_add_f32_e32 v231, v231, v86
	v_exp_f32_e32 v90, v90
	v_exp_f32_e32 v91, v91
	v_mfma_f32_32x32x16_f16 v[0:15], v[200:203], v[164:167], v[0:15]
	ds_read_b128 v[200:203], v226 offset:18528
	buffer_load_dword v222, v250, s[4:7], s25 offen
	v_cvt_pk_f16_f32 v173, v90, v91
	v_add_f32_e32 v90, v90, v91
	v_add_f32_e32 v231, v231, v88
	v_exp_f32_e32 v92, v92
	v_exp_f32_e32 v93, v93
	v_mfma_f32_32x32x16_f16 v[16:31], v[204:207], v[164:167], v[16:31]
	ds_read_b128 v[204:207], v226 offset:23136
	buffer_load_dword v223, v251, s[4:7], s25 offen
	v_cvt_pk_f16_f32 v174, v92, v93
	v_add_f32_e32 v92, v92, v93
	v_add_f32_e32 v231, v231, v90
	v_exp_f32_e32 v94, v94
	v_exp_f32_e32 v95, v95
	v_add_f32_e32 v231, v231, v92
	v_cvt_pk_f16_f32 v175, v94, v95
	v_add_f32_e32 v94, v94, v95
	v_add_f32_e32 v231, v231, v94
	v_cmp_nge_f32_e32 vcc, s34, v231
	s_cbranch_vccnz .Lovf_a1_21
.Lovfret_a1_21:
	v_add_f32_e32 v232, v232, v231
	s_waitcnt lgkmcnt(6)
	s_barrier
	s_add_u32 s23, s23, 1
	s_waitcnt vmcnt(8)
	v_cmp_ne_u32_e64 s[20:21], 0, v224
	s_add_u32 s31, s23, 1
	s_and_b32 s31, s31, 31
	s_lshl_b32 s31, s31, 8
	s_add_u32 s26, s31, s22
	s_add_u32 s31, s23, 3
	s_and_b32 s31, s31, 31
	s_mul_i32 s31, s31, 0xc0000
	s_add_u32 s24, s31, s18
	s_add_u32 s31, s23, 2
	s_and_b32 s31, s31, 31
	s_mul_i32 s31, s31, 0xc0000
	s_add_u32 s25, s31, s19
	s_cmp_eq_u64 s[20:21], -1
	s_cselect_b32 s34, s37, s38
	s_waitcnt lgkmcnt(4)
	v_mfma_f32_32x32x16_f16 v[80:95], v[176:179], v[128:131], v[96:111]
	ds_read_b128 v[176:179], v225 offset:0
	s_add_u32 s31, s29, 0xc48000
	buffer_load_dwordx4 v[56:59], v243, s[4:7], s31 offen nt
	s_add_u32 s31, s29, 0xc54000
	buffer_load_dwordx4 v[60:63], v243, s[4:7], s31 offen nt
	buffer_load_dword v224, v230, s[8:11], s26 offen
	v_exp_f32_e32 v64, v64
	v_exp_f32_e32 v65, v65
	v_cvt_pk_f16_f32 v208, v208, v209
	v_cvt_pk_f16_f32 v209, v210, v211
	v_mfma_f32_32x32x16_f16 v[80:95], v[180:183], v[132:135], v[80:95]
	ds_read_b128 v[180:183], v225 offset:32
	v_cvt_pk_f16_f32 v160, v64, v65
	v_add_f32_e32 v64, v64, v65
	v_cvt_pk_f16_f32 v212, v212, v213
	v_exp_f32_e32 v66, v66
	v_exp_f32_e32 v67, v67
	v_cvt_pk_f16_f32 v213, v214, v215
	v_mfma_f32_32x32x16_f16 v[80:95], v[184:187], v[136:139], v[80:95]
	ds_write_b64 v227, v[208:209] offset:9216
	ds_write_b64 v227, v[212:213] offset:13824
	ds_read_b128 v[184:187], v225 offset:64
	v_cvt_pk_f16_f32 v161, v66, v67
	v_add_f32_e32 v66, v66, v67
	v_exp_f32_e32 v68, v68
	v_exp_f32_e32 v69, v69
	v_mfma_f32_32x32x16_f16 v[80:95], v[188:191], v[140:143], v[80:95]
	ds_read_b128 v[188:191], v225 offset:96
	buffer_load_dwordx4 v[208:211], v229, s[4:7], s24 offen
	v_cvt_pk_f16_f32 v162, v68, v69
	v_add_f32_e32 v68, v68, v69
	v_add_f32_e32 v231, v64, v66
	v_exp_f32_e32 v70, v70
	v_exp_f32_e32 v71, v71
	s_waitcnt lgkmcnt(6)
	v_mfma_f32_32x32x16_f16 v[0:15], v[192:195], v[168:171], v[0:15]
	ds_read_b128 v[192:195], v226 offset:27648
	buffer_load_dwordx4 v[212:215], v252, s[4:7], s24 offen
	v_cvt_pk_f16_f32 v163, v70, v71
	v_add_f32_e32 v70, v70, v71
	v_add_f32_e32 v231, v231, v68
	v_exp_f32_e32 v72, v72
	v_exp_f32_e32 v73, v73
	v_mfma_f32_32x32x16_f16 v[16:31], v[196:199], v[168:171], v[16:31]
	ds_read_b128 v[196:199], v226 offset:32256
	v_cvt_pk_f16_f32 v164, v72, v73
	v_add_f32_e32 v72, v72, v73
	v_add_f32_e32 v231, v231, v70
	v_exp_f32_e32 v74, v74
	v_exp_f32_e32 v75, v75
	v_mfma_f32_32x32x16_f16 v[0:15], v[200:203], v[172:175], v[0:15]
	ds_read_b128 v[200:203], v226 offset:27680
	v_cvt_pk_f16_f32 v165, v74, v75
	v_add_f32_e32 v74, v74, v75
	v_add_f32_e32 v231, v231, v72
	v_exp_f32_e32 v76, v76
	v_exp_f32_e32 v77, v77
	v_mfma_f32_32x32x16_f16 v[16:31], v[204:207], v[172:175], v[16:31]
	ds_read_b128 v[204:207], v226 offset:32288
	v_cvt_pk_f16_f32 v166, v76, v77
	v_add_f32_e32 v76, v76, v77
	v_add_f32_e32 v231, v231, v74
	v_exp_f32_e32 v78, v78
	v_exp_f32_e32 v79, v79
	v_add_f32_e32 v231, v231, v76
	v_cvt_pk_f16_f32 v167, v78, v79
	v_add_f32_e32 v78, v78, v79
	v_add_f32_e32 v231, v231, v78
	v_cmp_nge_f32_e32 vcc, s34, v231
	s_cbranch_vccnz .Lovf_a1_30
.Lovfret_a1_30:
	v_add_f32_e32 v232, v232, v231
	s_waitcnt lgkmcnt(4)
	v_mfma_f32_32x32x16_f16 v[64:79], v[176:179], v[128:131], v[96:111]
	s_waitcnt vmcnt(5)
	v_exp_f32_e32 v80, v80
	v_exp_f32_e32 v81, v81
	v_cvt_pk_f16_f32 v216, v216, v217
	v_cvt_pk_f16_f32 v217, v218, v219
	v_mfma_f32_32x32x16_f16 v[64:79], v[180:183], v[132:135], v[64:79]
	v_cvt_pk_f16_f32 v168, v80, v81
	v_add_f32_e32 v80, v80, v81
	v_cvt_pk_f16_f32 v218, v220, v221
	v_exp_f32_e32 v82, v82
	v_exp_f32_e32 v83, v83
	v_cvt_pk_f16_f32 v219, v222, v223
	v_mfma_f32_32x32x16_f16 v[64:79], v[184:187], v[136:139], v[64:79]
	ds_write_b128 v228, v[216:219] offset:0
	v_cvt_pk_f16_f32 v169, v82, v83
	v_add_f32_e32 v82, v82, v83
	v_exp_f32_e32 v84, v84
	v_exp_f32_e32 v85, v85
	v_mfma_f32_32x32x16_f16 v[64:79], v[188:191], v[140:143], v[64:79]
	buffer_load_dword v216, v230, s[4:7], s25 offen
	buffer_load_dword v217, v245, s[4:7], s25 offen
	v_cvt_pk_f16_f32 v170, v84, v85
	v_add_f32_e32 v84, v84, v85
	v_add_f32_e32 v231, v80, v82
	v_exp_f32_e32 v86, v86
	v_exp_f32_e32 v87, v87
	s_waitcnt lgkmcnt(1)
	v_mfma_f32_32x32x16_f16 v[0:15], v[192:195], v[160:163], v[0:15]
	ds_read_b128 v[192:195], v226 offset:27712
	buffer_load_dword v218, v246, s[4:7], s25 offen
	buffer_load_dword v219, v247, s[4:7], s25 offen
	v_cvt_pk_f16_f32 v171, v86, v87
	v_add_f32_e32 v86, v86, v87
	v_add_f32_e32 v231, v231, v84
	v_exp_f32_e32 v88, v88
	v_exp_f32_e32 v89, v89
	v_mfma_f32_32x32x16_f16 v[16:31], v[196:199], v[160:163], v[16:31]
	ds_read_b128 v[196:199], v226 offset:32320
	buffer_load_dword v220, v248, s[4:7], s25 offen
	buffer_load_dword v221, v249, s[4:7], s25 offen
	v_cvt_pk_f16_f32 v172, v88, v89
	v_add_f32_e32 v88, v88, v89
	v_add_f32_e32 v231, v231, v86
	v_exp_f32_e32 v90, v90
	v_exp_f32_e32 v91, v91
	v_mfma_f32_32x32x16_f16 v[0:15], v[200:203], v[164:167], v[0:15]
	ds_read_b128 v[200:203], v226 offset:27744
	buffer_load_dword v222, v250, s[4:7], s25 offen
	v_cvt_pk_f16_f32 v173, v90, v91
	v_add_f32_e32 v90, v90, v91
	v_add_f32_e32 v231, v231, v88
	v_exp_f32_e32 v92, v92
	v_exp_f32_e32 v93, v93
	v_mfma_f32_32x32x16_f16 v[16:31], v[204:207], v[164:167], v[16:31]
	ds_read_b128 v[204:207], v226 offset:32352
	buffer_load_dword v223, v251, s[4:7], s25 offen
	v_cvt_pk_f16_f32 v174, v92, v93
	v_add_f32_e32 v92, v92, v93
	v_add_f32_e32 v231, v231, v90
	v_exp_f32_e32 v94, v94
	v_exp_f32_e32 v95, v95
	v_add_f32_e32 v231, v231, v92
	v_cvt_pk_f16_f32 v175, v94, v95
	v_add_f32_e32 v94, v94, v95
	v_add_f32_e32 v231, v231, v94
	v_cmp_nge_f32_e32 vcc, s34, v231
	s_cbranch_vccnz .Lovf_a1_31

.Lovfret_b31:
	v_add_f32_e32 v233, v233, v231
	s_waitcnt lgkmcnt(6)
	s_barrier
	s_add_u32 s23, s23, 1
	s_add_u32 s27, s27, 1
	s_cmp_eq_u32 s27, 7
	s_cbranch_scc0 .Lbody
	s_nop 15
	s_nop 7
	v_mov_b32_e32 v235, v232
	v_mov_b32_e32 v236, v232
	s_nop 1
	v_permlane32_swap_b32_e32 v235, v236
	v_add_f32_e32 v236, v235, v236
	v_rcp_f32_e32 v237, v236
	s_nop 0
	v_fma_f32 v238, -v236, v237, 1.0
	v_fmac_f32_e32 v237, v238, v237
	v_mul_f32_e32 v0, v237, v0
	v_mul_f32_e32 v1, v237, v1
	v_mul_f32_e32 v2, v237, v2
	v_mul_f32_e32 v3, v237, v3
	v_mul_f32_e32 v4, v237, v4
	v_mul_f32_e32 v5, v237, v5
	v_mul_f32_e32 v6, v237, v6
	v_mul_f32_e32 v7, v237, v7
	v_mul_f32_e32 v8, v237, v8
	v_mul_f32_e32 v9, v237, v9
	v_mul_f32_e32 v10, v237, v10
	v_mul_f32_e32 v11, v237, v11
	v_mul_f32_e32 v12, v237, v12
	v_mul_f32_e32 v13, v237, v13
	v_mul_f32_e32 v14, v237, v14
	v_mul_f32_e32 v15, v237, v15
	v_mul_f32_e32 v16, v237, v16
	v_mul_f32_e32 v17, v237, v17
	v_mul_f32_e32 v18, v237, v18
	v_mul_f32_e32 v19, v237, v19
	v_mul_f32_e32 v20, v237, v20
	v_mul_f32_e32 v21, v237, v21
	v_mul_f32_e32 v22, v237, v22
	v_mul_f32_e32 v23, v237, v23
	v_mul_f32_e32 v24, v237, v24
	v_mul_f32_e32 v25, v237, v25
	v_mul_f32_e32 v26, v237, v26
	v_mul_f32_e32 v27, v237, v27
	v_mul_f32_e32 v28, v237, v28
	v_mul_f32_e32 v29, v237, v29
	v_mul_f32_e32 v30, v237, v30
	v_mul_f32_e32 v31, v237, v31
	ds_write_b128 v241, v[0:3] offset:0
	ds_write_b128 v241, v[16:19] offset:128
	ds_write_b128 v241, v[4:7] offset:32
	ds_write_b128 v241, v[20:23] offset:160
	ds_write_b128 v241, v[8:11] offset:64
	ds_write_b128 v241, v[24:27] offset:192
	ds_write_b128 v241, v[12:15] offset:96
	ds_write_b128 v241, v[28:31] offset:224
	s_waitcnt lgkmcnt(0)
	ds_read_b128 v[0:3], v242 offset:0
	ds_read_b128 v[4:7], v242 offset:1088
	ds_read_b128 v[8:11], v242 offset:2176
	ds_read_b128 v[12:15], v242 offset:3264
	ds_read_b128 v[16:19], v242 offset:4352
	ds_read_b128 v[20:23], v242 offset:5440
	ds_read_b128 v[24:27], v242 offset:6528
	ds_read_b128 v[28:31], v242 offset:7616
	s_waitcnt lgkmcnt(7)
	s_add_u32 s31, s30, 0x0
	buffer_store_dwordx4 v[0:3], v244, s[12:15], s31 offen nt sc1
	s_waitcnt lgkmcnt(6)
	s_add_u32 s31, s30, 0x4000
	buffer_store_dwordx4 v[4:7], v244, s[12:15], s31 offen nt sc1
	s_waitcnt lgkmcnt(5)
	s_add_u32 s31, s30, 0x8000
	buffer_store_dwordx4 v[8:11], v244, s[12:15], s31 offen nt sc1
	s_waitcnt lgkmcnt(4)
	s_add_u32 s31, s30, 0xc000
	buffer_store_dwordx4 v[12:15], v244, s[12:15], s31 offen nt sc1
	s_waitcnt lgkmcnt(3)
	s_add_u32 s31, s30, 0x10000
	buffer_store_dwordx4 v[16:19], v244, s[12:15], s31 offen nt sc1
	s_waitcnt lgkmcnt(2)
	s_add_u32 s31, s30, 0x14000
	buffer_store_dwordx4 v[20:23], v244, s[12:15], s31 offen nt sc1
	s_waitcnt lgkmcnt(1)
	s_add_u32 s31, s30, 0x18000
	buffer_store_dwordx4 v[24:27], v244, s[12:15], s31 offen nt sc1
	s_waitcnt lgkmcnt(0)
	s_add_u32 s31, s30, 0x1c000
	buffer_store_dwordx4 v[28:31], v244, s[12:15], s31 offen nt sc1
	s_nop 1
	s_waitcnt lgkmcnt(0)
	v_mfma_f32_32x32x16_f16 v[80:95], v[176:179], v[144:147], v[112:127]
	ds_read_b128 v[176:179], v225 offset:4608
	v_mfma_f32_32x32x16_f16 v[80:95], v[180:183], v[148:151], v[80:95]
	ds_read_b128 v[180:183], v225 offset:4640
	v_mfma_f32_32x32x16_f16 v[80:95], v[184:187], v[152:155], v[80:95]
	ds_read_b128 v[184:187], v225 offset:4672
	v_mfma_f32_32x32x16_f16 v[80:95], v[188:191], v[156:159], v[80:95]
	ds_read_b128 v[188:191], v225 offset:4704
	s_nop 15
	s_nop 3
	s_waitcnt vmcnt(8)
	v_cmp_ne_u32_e64 s[20:21], 0, v224
	s_add_u32 s31, s23, 1
	s_and_b32 s31, s31, 31
	s_lshl_b32 s31, s31, 8
	s_add_u32 s26, s31, s22
	s_add_u32 s31, s23, 3
	s_and_b32 s31, s31, 31
	s_mul_i32 s31, s31, 0xc0000
	s_add_u32 s24, s31, s18
	s_add_u32 s31, s23, 2
	s_and_b32 s31, s31, 31
	s_mul_i32 s31, s31, 0xc0000
	s_add_u32 s25, s31, s19
	s_cmp_eq_u64 s[20:21], -1
	s_cselect_b32 s34, s37, s38
	s_waitcnt lgkmcnt(0)
	v_mfma_f32_32x32x16_f16 v[64:79], v[176:179], v[144:147], v[112:127]
	ds_read_b128 v[176:179], v225 offset:9216
	buffer_load_dword v224, v230, s[8:11], s26 offen
	v_exp_f32_e32 v80, v80
	v_exp_f32_e32 v81, v81
	v_cvt_pk_f16_f32 v208, v208, v209
	v_cvt_pk_f16_f32 v209, v210, v211
	v_mfma_f32_32x32x16_f16 v[64:79], v[180:183], v[148:151], v[64:79]
	ds_read_b128 v[180:183], v225 offset:9248
	v_cvt_pk_f16_f32 v160, v80, v81
	v_add_f32_e32 v80, v80, v81
	v_cvt_pk_f16_f32 v212, v212, v213
	v_exp_f32_e32 v82, v82
	v_exp_f32_e32 v83, v83
	v_cvt_pk_f16_f32 v213, v214, v215
	v_mfma_f32_32x32x16_f16 v[64:79], v[184:187], v[152:155], v[64:79]
	ds_write_b64 v227, v[208:209] offset:18432
	ds_write_b64 v227, v[212:213] offset:23040
	ds_read_b128 v[184:187], v225 offset:9280
	v_cvt_pk_f16_f32 v161, v82, v83
	v_add_f32_e32 v82, v82, v83
	v_exp_f32_e32 v84, v84
	v_exp_f32_e32 v85, v85
	v_mfma_f32_32x32x16_f16 v[64:79], v[188:191], v[156:159], v[64:79]
	ds_read_b128 v[188:191], v225 offset:9312
	buffer_load_dwordx4 v[208:211], v229, s[4:7], s24 offen
	v_cvt_pk_f16_f32 v162, v84, v85
	v_add_f32_e32 v84, v84, v85
	v_add_f32_e32 v231, v80, v82
	v_exp_f32_e32 v86, v86
	v_exp_f32_e32 v87, v87
	s_waitcnt lgkmcnt(10)
	v_mfma_f32_32x32x16_f16 v[32:47], v[192:195], v[168:171], v[32:47]
	ds_read_b128 v[192:195], v226 offset:0
	buffer_load_dwordx4 v[212:215], v252, s[4:7], s24 offen
	v_cvt_pk_f16_f32 v163, v86, v87
	v_add_f32_e32 v86, v86, v87
	v_add_f32_e32 v231, v231, v84
	v_exp_f32_e32 v88, v88
	v_exp_f32_e32 v89, v89
	v_mfma_f32_32x32x16_f16 v[48:63], v[196:199], v[168:171], v[48:63]
	ds_read_b128 v[196:199], v226 offset:4608
	v_cvt_pk_f16_f32 v164, v88, v89
	v_add_f32_e32 v88, v88, v89
	v_add_f32_e32 v231, v231, v86
	v_exp_f32_e32 v90, v90
	v_exp_f32_e32 v91, v91
	v_mfma_f32_32x32x16_f16 v[32:47], v[200:203], v[172:175], v[32:47]
	ds_read_b128 v[200:203], v226 offset:32
	v_cvt_pk_f16_f32 v165, v90, v91
	v_add_f32_e32 v90, v90, v91
	v_add_f32_e32 v231, v231, v88
	v_exp_f32_e32 v92, v92
	v_exp_f32_e32 v93, v93
	v_mfma_f32_32x32x16_f16 v[48:63], v[204:207], v[172:175], v[48:63]
	ds_read_b128 v[204:207], v226 offset:4640
	v_cvt_pk_f16_f32 v166, v92, v93
	v_add_f32_e32 v92, v92, v93
	v_add_f32_e32 v231, v231, v90
	v_exp_f32_e32 v94, v94
	v_exp_f32_e32 v95, v95
	v_add_f32_e32 v231, v231, v92
	v_cvt_pk_f16_f32 v167, v94, v95
	v_add_f32_e32 v94, v94, v95
	v_add_f32_e32 v231, v231, v94
	v_cmp_nge_f32_e32 vcc, s34, v231
	s_cbranch_vccnz .Lovf_b1_00
.Lovfret_b1_00:
	v_add_f32_e32 v233, v233, v231
	s_waitcnt lgkmcnt(4)
	v_mfma_f32_32x32x16_f16 v[80:95], v[176:179], v[144:147], v[112:127]
	ds_read_b128 v[176:179], v225 offset:13824
	s_waitcnt vmcnt(3)
	v_exp_f32_e32 v64, v64
	v_exp_f32_e32 v65, v65
	v_cvt_pk_f16_f32 v216, v216, v217
	v_cvt_pk_f16_f32 v217, v218, v219
	v_mfma_f32_32x32x16_f16 v[80:95], v[180:183], v[148:151], v[80:95]
	ds_read_b128 v[180:183], v225 offset:13856
	v_cvt_pk_f16_f32 v168, v64, v65
	v_add_f32_e32 v64, v64, v65
	v_cvt_pk_f16_f32 v218, v220, v221
	v_exp_f32_e32 v66, v66
	v_exp_f32_e32 v67, v67
	v_cvt_pk_f16_f32 v219, v222, v223
	v_mfma_f32_32x32x16_f16 v[80:95], v[184:187], v[152:155], v[80:95]
	ds_write_b128 v228, v[216:219] offset:9216
	ds_read_b128 v[184:187], v225 offset:13888
	v_cvt_pk_f16_f32 v169, v66, v67
	v_add_f32_e32 v66, v66, v67
	v_exp_f32_e32 v68, v68
	v_exp_f32_e32 v69, v69
	v_mfma_f32_32x32x16_f16 v[80:95], v[188:191], v[156:159], v[80:95]
	ds_read_b128 v[188:191], v225 offset:13920
	buffer_load_dword v216, v230, s[4:7], s25 offen
	buffer_load_dword v217, v245, s[4:7], s25 offen
	v_cvt_pk_f16_f32 v170, v68, v69
	v_add_f32_e32 v68, v68, v69
	v_add_f32_e32 v231, v64, v66
	v_exp_f32_e32 v70, v70
	v_exp_f32_e32 v71, v71
	s_waitcnt lgkmcnt(5)
	v_mfma_f32_32x32x16_f16 v[32:47], v[192:195], v[160:163], v[32:47]
	ds_read_b128 v[192:195], v226 offset:64
	buffer_load_dword v218, v246, s[4:7], s25 offen
	buffer_load_dword v219, v247, s[4:7], s25 offen
	v_cvt_pk_f16_f32 v171, v70, v71
	v_add_f32_e32 v70, v70, v71
	v_add_f32_e32 v231, v231, v68
	v_exp_f32_e32 v72, v72
	v_exp_f32_e32 v73, v73
	v_mfma_f32_32x32x16_f16 v[48:63], v[196:199], v[160:163], v[48:63]
	ds_read_b128 v[196:199], v226 offset:4672
	buffer_load_dword v220, v248, s[4:7], s25 offen
	buffer_load_dword v221, v249, s[4:7], s25 offen
	v_cvt_pk_f16_f32 v172, v72, v73
	v_add_f32_e32 v72, v72, v73
	v_add_f32_e32 v231, v231, v70
	v_exp_f32_e32 v74, v74
	v_exp_f32_e32 v75, v75
	v_mfma_f32_32x32x16_f16 v[32:47], v[200:203], v[164:167], v[32:47]
	ds_read_b128 v[200:203], v226 offset:96
	buffer_load_dword v222, v250, s[4:7], s25 offen
	v_cvt_pk_f16_f32 v173, v74, v75
	v_add_f32_e32 v74, v74, v75
	v_add_f32_e32 v231, v231, v72
	v_exp_f32_e32 v76, v76
	v_exp_f32_e32 v77, v77
	v_mfma_f32_32x32x16_f16 v[48:63], v[204:207], v[164:167], v[48:63]
	ds_read_b128 v[204:207], v226 offset:4704
	buffer_load_dword v223, v251, s[4:7], s25 offen
	v_cvt_pk_f16_f32 v174, v76, v77
	v_add_f32_e32 v76, v76, v77
	v_add_f32_e32 v231, v231, v74
	v_exp_f32_e32 v78, v78
	v_exp_f32_e32 v79, v79
	v_add_f32_e32 v231, v231, v76
	v_cvt_pk_f16_f32 v175, v78, v79
	v_add_f32_e32 v78, v78, v79
	v_add_f32_e32 v231, v231, v78
	v_cmp_nge_f32_e32 vcc, s34, v231
	s_cbranch_vccnz .Lovf_b1_01
.Lovfret_b1_01:
	v_add_f32_e32 v233, v233, v231
	s_waitcnt lgkmcnt(6)
	s_barrier
	s_add_u32 s23, s23, 1
	s_waitcnt vmcnt(8)
	v_cmp_ne_u32_e64 s[20:21], 0, v224
	s_add_u32 s31, s23, 1
	s_and_b32 s31, s31, 31
	s_lshl_b32 s31, s31, 8
	s_add_u32 s26, s31, s22
	s_add_u32 s31, s23, 3
	s_and_b32 s31, s31, 31
	s_mul_i32 s31, s31, 0xc0000
	s_add_u32 s24, s31, s18
	s_add_u32 s31, s23, 2
	s_and_b32 s31, s31, 31
	s_mul_i32 s31, s31, 0xc0000
	s_add_u32 s25, s31, s19
	s_cmp_eq_u64 s[20:21], -1
	s_cselect_b32 s34, s37, s38
	s_waitcnt lgkmcnt(4)
	v_mfma_f32_32x32x16_f16 v[64:79], v[176:179], v[144:147], v[112:127]
	ds_read_b128 v[176:179], v225 offset:18432
	buffer_load_dword v224, v230, s[8:11], s26 offen
	v_exp_f32_e32 v80, v80
	v_exp_f32_e32 v81, v81
	v_cvt_pk_f16_f32 v208, v208, v209
	v_cvt_pk_f16_f32 v209, v210, v211
	v_mfma_f32_32x32x16_f16 v[64:79], v[180:183], v[148:151], v[64:79]
	ds_read_b128 v[180:183], v225 offset:18464
	v_cvt_pk_f16_f32 v160, v80, v81
	v_add_f32_e32 v80, v80, v81
	v_cvt_pk_f16_f32 v212, v212, v213
	v_exp_f32_e32 v82, v82
	v_exp_f32_e32 v83, v83
	v_cvt_pk_f16_f32 v213, v214, v215
	v_mfma_f32_32x32x16_f16 v[64:79], v[184:187], v[152:155], v[64:79]
	ds_write_b64 v227, v[208:209] offset:27648
	ds_write_b64 v227, v[212:213] offset:32256
	ds_read_b128 v[184:187], v225 offset:18496
	v_cvt_pk_f16_f32 v161, v82, v83
	v_add_f32_e32 v82, v82, v83
	v_exp_f32_e32 v84, v84
	v_exp_f32_e32 v85, v85
	v_mfma_f32_32x32x16_f16 v[64:79], v[188:191], v[156:159], v[64:79]
	ds_read_b128 v[188:191], v225 offset:18528
	buffer_load_dwordx4 v[208:211], v229, s[4:7], s24 offen
	v_cvt_pk_f16_f32 v162, v84, v85
	v_add_f32_e32 v84, v84, v85
	v_add_f32_e32 v231, v80, v82
	v_exp_f32_e32 v86, v86
	v_exp_f32_e32 v87, v87
	s_waitcnt lgkmcnt(6)
	v_mfma_f32_32x32x16_f16 v[32:47], v[192:195], v[168:171], v[32:47]
	ds_read_b128 v[192:195], v226 offset:9216
	buffer_load_dwordx4 v[212:215], v252, s[4:7], s24 offen
	v_cvt_pk_f16_f32 v163, v86, v87
	v_add_f32_e32 v86, v86, v87
	v_add_f32_e32 v231, v231, v84
	v_exp_f32_e32 v88, v88
	v_exp_f32_e32 v89, v89
	v_mfma_f32_32x32x16_f16 v[48:63], v[196:199], v[168:171], v[48:63]
	ds_read_b128 v[196:199], v226 offset:13824
	v_cvt_pk_f16_f32 v164, v88, v89
	v_add_f32_e32 v88, v88, v89
	v_add_f32_e32 v231, v231, v86
	v_exp_f32_e32 v90, v90
	v_exp_f32_e32 v91, v91
	v_mfma_f32_32x32x16_f16 v[32:47], v[200:203], v[172:175], v[32:47]
	ds_read_b128 v[200:203], v226 offset:9248
	v_cvt_pk_f16_f32 v165, v90, v91
	v_add_f32_e32 v90, v90, v91
	v_add_f32_e32 v231, v231, v88
	v_exp_f32_e32 v92, v92
	v_exp_f32_e32 v93, v93
	v_mfma_f32_32x32x16_f16 v[48:63], v[204:207], v[172:175], v[48:63]
	ds_read_b128 v[204:207], v226 offset:13856
	v_cvt_pk_f16_f32 v166, v92, v93
	v_add_f32_e32 v92, v92, v93
	v_add_f32_e32 v231, v231, v90
	v_exp_f32_e32 v94, v94
	v_exp_f32_e32 v95, v95
	v_add_f32_e32 v231, v231, v92
	v_cvt_pk_f16_f32 v167, v94, v95
	v_add_f32_e32 v94, v94, v95
	v_add_f32_e32 v231, v231, v94
	v_cmp_nge_f32_e32 vcc, s34, v231
	s_cbranch_vccnz .Lovf_b1_10
.Lovfret_b1_10:
	v_add_f32_e32 v233, v233, v231
	s_waitcnt lgkmcnt(4)
	v_mfma_f32_32x32x16_f16 v[80:95], v[176:179], v[144:147], v[112:127]
	ds_read_b128 v[176:179], v225 offset:23040
	s_waitcnt vmcnt(3)
	v_exp_f32_e32 v64, v64
	v_exp_f32_e32 v65, v65
	v_cvt_pk_f16_f32 v216, v216, v217
	v_cvt_pk_f16_f32 v217, v218, v219
	v_mfma_f32_32x32x16_f16 v[80:95], v[180:183], v[148:151], v[80:95]
	ds_read_b128 v[180:183], v225 offset:23072
	v_cvt_pk_f16_f32 v168, v64, v65
	v_add_f32_e32 v64, v64, v65
	v_cvt_pk_f16_f32 v218, v220, v221
	v_exp_f32_e32 v66, v66
	v_exp_f32_e32 v67, v67
	v_cvt_pk_f16_f32 v219, v222, v223
	v_mfma_f32_32x32x16_f16 v[80:95], v[184:187], v[152:155], v[80:95]
	ds_write_b128 v228, v[216:219] offset:18432
	ds_read_b128 v[184:187], v225 offset:23104
	v_cvt_pk_f16_f32 v169, v66, v67
	v_add_f32_e32 v66, v66, v67
	v_exp_f32_e32 v68, v68
	v_exp_f32_e32 v69, v69
	v_mfma_f32_32x32x16_f16 v[80:95], v[188:191], v[156:159], v[80:95]
	ds_read_b128 v[188:191], v225 offset:23136
	buffer_load_dword v216, v230, s[4:7], s25 offen
	buffer_load_dword v217, v245, s[4:7], s25 offen
	v_cvt_pk_f16_f32 v170, v68, v69
	v_add_f32_e32 v68, v68, v69
	v_add_f32_e32 v231, v64, v66
	v_exp_f32_e32 v70, v70
	v_exp_f32_e32 v71, v71
	s_waitcnt lgkmcnt(5)
	v_mfma_f32_32x32x16_f16 v[32:47], v[192:195], v[160:163], v[32:47]
	ds_read_b128 v[192:195], v226 offset:9280
	buffer_load_dword v218, v246, s[4:7], s25 offen
	buffer_load_dword v219, v247, s[4:7], s25 offen
	v_cvt_pk_f16_f32 v171, v70, v71
	v_add_f32_e32 v70, v70, v71
	v_add_f32_e32 v231, v231, v68
	v_exp_f32_e32 v72, v72
	v_exp_f32_e32 v73, v73
	v_mfma_f32_32x32x16_f16 v[48:63], v[196:199], v[160:163], v[48:63]
	ds_read_b128 v[196:199], v226 offset:13888
	buffer_load_dword v220, v248, s[4:7], s25 offen
	buffer_load_dword v221, v249, s[4:7], s25 offen
	v_cvt_pk_f16_f32 v172, v72, v73
	v_add_f32_e32 v72, v72, v73
	v_add_f32_e32 v231, v231, v70
	v_exp_f32_e32 v74, v74
	v_exp_f32_e32 v75, v75
	v_mfma_f32_32x32x16_f16 v[32:47], v[200:203], v[164:167], v[32:47]
	ds_read_b128 v[200:203], v226 offset:9312
	buffer_load_dword v222, v250, s[4:7], s25 offen
	v_cvt_pk_f16_f32 v173, v74, v75
	v_add_f32_e32 v74, v74, v75
	v_add_f32_e32 v231, v231, v72
	v_exp_f32_e32 v76, v76
	v_exp_f32_e32 v77, v77
	v_mfma_f32_32x32x16_f16 v[48:63], v[204:207], v[164:167], v[48:63]
	ds_read_b128 v[204:207], v226 offset:13920
	buffer_load_dword v223, v251, s[4:7], s25 offen
	v_cvt_pk_f16_f32 v174, v76, v77
	v_add_f32_e32 v76, v76, v77
	v_add_f32_e32 v231, v231, v74
	v_exp_f32_e32 v78, v78
	v_exp_f32_e32 v79, v79
	v_add_f32_e32 v231, v231, v76
	v_cvt_pk_f16_f32 v175, v78, v79
	v_add_f32_e32 v78, v78, v79
	v_add_f32_e32 v231, v231, v78
	v_cmp_nge_f32_e32 vcc, s34, v231
	s_cbranch_vccnz .Lovf_b1_11
.Lovfret_b1_11:
	v_add_f32_e32 v233, v233, v231
	s_waitcnt lgkmcnt(6)
	s_barrier
	s_add_u32 s23, s23, 1
	s_waitcnt vmcnt(8)
	v_cmp_ne_u32_e64 s[20:21], 0, v224
	s_add_u32 s31, s23, 1
	s_and_b32 s31, s31, 31
	s_lshl_b32 s31, s31, 8
	s_add_u32 s26, s31, s22
	s_add_u32 s31, s23, 3
	s_and_b32 s31, s31, 31
	s_mul_i32 s31, s31, 0xc0000
	s_add_u32 s24, s31, s18
	s_add_u32 s31, s23, 2
	s_and_b32 s31, s31, 31
	s_mul_i32 s31, s31, 0xc0000
	s_add_u32 s25, s31, s19
	s_cmp_eq_u64 s[20:21], -1
	s_cselect_b32 s34, s37, s38
	s_waitcnt lgkmcnt(4)
	v_mfma_f32_32x32x16_f16 v[64:79], v[176:179], v[144:147], v[112:127]
	ds_read_b128 v[176:179], v225 offset:27648
	buffer_load_dword v224, v230, s[8:11], s26 offen
	v_exp_f32_e32 v80, v80
	v_exp_f32_e32 v81, v81
	v_cvt_pk_f16_f32 v208, v208, v209
	v_cvt_pk_f16_f32 v209, v210, v211
	v_mfma_f32_32x32x16_f16 v[64:79], v[180:183], v[148:151], v[64:79]
	ds_read_b128 v[180:183], v225 offset:27680
	v_cvt_pk_f16_f32 v160, v80, v81
	v_add_f32_e32 v80, v80, v81
	v_cvt_pk_f16_f32 v212, v212, v213
	v_exp_f32_e32 v82, v82
	v_exp_f32_e32 v83, v83
	v_cvt_pk_f16_f32 v213, v214, v215
	v_mfma_f32_32x32x16_f16 v[64:79], v[184:187], v[152:155], v[64:79]
	ds_write_b64 v227, v[208:209] offset:0
	ds_write_b64 v227, v[212:213] offset:4608
	ds_read_b128 v[184:187], v225 offset:27712
	v_cvt_pk_f16_f32 v161, v82, v83
	v_add_f32_e32 v82, v82, v83
	v_exp_f32_e32 v84, v84
	v_exp_f32_e32 v85, v85
	v_mfma_f32_32x32x16_f16 v[64:79], v[188:191], v[156:159], v[64:79]
	ds_read_b128 v[188:191], v225 offset:27744
	buffer_load_dwordx4 v[208:211], v229, s[4:7], s24 offen
	v_cvt_pk_f16_f32 v162, v84, v85
	v_add_f32_e32 v84, v84, v85
	v_add_f32_e32 v231, v80, v82
	v_exp_f32_e32 v86, v86
	v_exp_f32_e32 v87, v87
	s_waitcnt lgkmcnt(6)
	v_mfma_f32_32x32x16_f16 v[32:47], v[192:195], v[168:171], v[32:47]
	ds_read_b128 v[192:195], v226 offset:18432
	buffer_load_dwordx4 v[212:215], v252, s[4:7], s24 offen
	v_cvt_pk_f16_f32 v163, v86, v87
	v_add_f32_e32 v86, v86, v87
	v_add_f32_e32 v231, v231, v84
	v_exp_f32_e32 v88, v88
	v_exp_f32_e32 v89, v89
	v_mfma_f32_32x32x16_f16 v[48:63], v[196:199], v[168:171], v[48:63]
	ds_read_b128 v[196:199], v226 offset:23040
	v_cvt_pk_f16_f32 v164, v88, v89
	v_add_f32_e32 v88, v88, v89
	v_add_f32_e32 v231, v231, v86
	v_exp_f32_e32 v90, v90
	v_exp_f32_e32 v91, v91
	v_mfma_f32_32x32x16_f16 v[32:47], v[200:203], v[172:175], v[32:47]
	ds_read_b128 v[200:203], v226 offset:18464
	v_cvt_pk_f16_f32 v165, v90, v91
	v_add_f32_e32 v90, v90, v91
	v_add_f32_e32 v231, v231, v88
	v_exp_f32_e32 v92, v92
	v_exp_f32_e32 v93, v93
	v_mfma_f32_32x32x16_f16 v[48:63], v[204:207], v[172:175], v[48:63]
	ds_read_b128 v[204:207], v226 offset:23072
	v_cvt_pk_f16_f32 v166, v92, v93
	v_add_f32_e32 v92, v92, v93
	v_add_f32_e32 v231, v231, v90
	v_exp_f32_e32 v94, v94
	v_exp_f32_e32 v95, v95
	v_add_f32_e32 v231, v231, v92
	v_cvt_pk_f16_f32 v167, v94, v95
	v_add_f32_e32 v94, v94, v95
	v_add_f32_e32 v231, v231, v94
	v_cmp_nge_f32_e32 vcc, s34, v231
	s_cbranch_vccnz .Lovf_b1_20
.Lovfret_b1_20:
	v_add_f32_e32 v233, v233, v231
	s_waitcnt lgkmcnt(4)
	v_mfma_f32_32x32x16_f16 v[80:95], v[176:179], v[144:147], v[112:127]
	ds_read_b128 v[176:179], v225 offset:32256
	s_waitcnt vmcnt(3)
	v_exp_f32_e32 v64, v64
	v_exp_f32_e32 v65, v65
	v_cvt_pk_f16_f32 v216, v216, v217
	v_cvt_pk_f16_f32 v217, v218, v219
	v_mfma_f32_32x32x16_f16 v[80:95], v[180:183], v[148:151], v[80:95]
	ds_read_b128 v[180:183], v225 offset:32288
	v_cvt_pk_f16_f32 v168, v64, v65
	v_add_f32_e32 v64, v64, v65
	v_cvt_pk_f16_f32 v218, v220, v221
	v_exp_f32_e32 v66, v66
	v_exp_f32_e32 v67, v67
	v_cvt_pk_f16_f32 v219, v222, v223
	v_mfma_f32_32x32x16_f16 v[80:95], v[184:187], v[152:155], v[80:95]
	ds_write_b128 v228, v[216:219] offset:27648
	ds_read_b128 v[184:187], v225 offset:32320
	v_cvt_pk_f16_f32 v169, v66, v67
	v_add_f32_e32 v66, v66, v67
	v_exp_f32_e32 v68, v68
	v_exp_f32_e32 v69, v69
	v_mfma_f32_32x32x16_f16 v[80:95], v[188:191], v[156:159], v[80:95]
	ds_read_b128 v[188:191], v225 offset:32352
	buffer_load_dword v216, v230, s[4:7], s25 offen
	buffer_load_dword v217, v245, s[4:7], s25 offen
	v_cvt_pk_f16_f32 v170, v68, v69
	v_add_f32_e32 v68, v68, v69
	v_add_f32_e32 v231, v64, v66
	v_exp_f32_e32 v70, v70
	v_exp_f32_e32 v71, v71
	s_waitcnt lgkmcnt(5)
	v_mfma_f32_32x32x16_f16 v[32:47], v[192:195], v[160:163], v[32:47]
	ds_read_b128 v[192:195], v226 offset:18496
	buffer_load_dword v218, v246, s[4:7], s25 offen
	buffer_load_dword v219, v247, s[4:7], s25 offen
	v_cvt_pk_f16_f32 v171, v70, v71
	v_add_f32_e32 v70, v70, v71
	v_add_f32_e32 v231, v231, v68
	v_exp_f32_e32 v72, v72
	v_exp_f32_e32 v73, v73
	v_mfma_f32_32x32x16_f16 v[48:63], v[196:199], v[160:163], v[48:63]
	ds_read_b128 v[196:199], v226 offset:23104
	buffer_load_dword v220, v248, s[4:7], s25 offen
	buffer_load_dword v221, v249, s[4:7], s25 offen
	v_cvt_pk_f16_f32 v172, v72, v73
	v_add_f32_e32 v72, v72, v73
	v_add_f32_e32 v231, v231, v70
	v_exp_f32_e32 v74, v74
	v_exp_f32_e32 v75, v75
	v_mfma_f32_32x32x16_f16 v[32:47], v[200:203], v[164:167], v[32:47]
	ds_read_b128 v[200:203], v226 offset:18528
	buffer_load_dword v222, v250, s[4:7], s25 offen
	v_cvt_pk_f16_f32 v173, v74, v75
	v_add_f32_e32 v74, v74, v75
	v_add_f32_e32 v231, v231, v72
	v_exp_f32_e32 v76, v76
	v_exp_f32_e32 v77, v77
	v_mfma_f32_32x32x16_f16 v[48:63], v[204:207], v[164:167], v[48:63]
	ds_read_b128 v[204:207], v226 offset:23136
	buffer_load_dword v223, v251, s[4:7], s25 offen
	v_cvt_pk_f16_f32 v174, v76, v77
	v_add_f32_e32 v76, v76, v77
	v_add_f32_e32 v231, v231, v74
	v_exp_f32_e32 v78, v78
	v_exp_f32_e32 v79, v79
	v_add_f32_e32 v231, v231, v76
	v_cvt_pk_f16_f32 v175, v78, v79
	v_add_f32_e32 v78, v78, v79
	v_add_f32_e32 v231, v231, v78
	v_cmp_nge_f32_e32 vcc, s34, v231
	s_cbranch_vccnz .Lovf_b1_21
.Lovfret_b1_21:
	v_add_f32_e32 v233, v233, v231
	s_waitcnt lgkmcnt(6)
	s_barrier
	s_add_u32 s23, s23, 1
	s_waitcnt vmcnt(8)
	v_cmp_ne_u32_e64 s[20:21], 0, v224
	s_add_u32 s31, s23, 1
	s_and_b32 s31, s31, 31
	s_lshl_b32 s31, s31, 8
	s_add_u32 s26, s31, s22
	s_add_u32 s31, s23, 3
	s_and_b32 s31, s31, 31
	s_mul_i32 s31, s31, 0xc0000
	s_add_u32 s24, s31, s18
	s_add_u32 s31, s23, 2
	s_and_b32 s31, s31, 31
	s_mul_i32 s31, s31, 0xc0000
	s_add_u32 s25, s31, s19
	s_cmp_eq_u64 s[20:21], -1
	s_cselect_b32 s34, s37, s38
	s_waitcnt lgkmcnt(4)
	v_mfma_f32_32x32x16_f16 v[64:79], v[176:179], v[144:147], v[112:127]
	ds_read_b128 v[176:179], v225 offset:0
	buffer_load_dword v224, v230, s[8:11], s26 offen
	v_exp_f32_e32 v80, v80
	v_exp_f32_e32 v81, v81
	v_cvt_pk_f16_f32 v208, v208, v209
	v_cvt_pk_f16_f32 v209, v210, v211
	v_mfma_f32_32x32x16_f16 v[64:79], v[180:183], v[148:151], v[64:79]
	ds_read_b128 v[180:183], v225 offset:32
	v_cvt_pk_f16_f32 v160, v80, v81
	v_add_f32_e32 v80, v80, v81
	v_cvt_pk_f16_f32 v212, v212, v213
	v_exp_f32_e32 v82, v82
	v_exp_f32_e32 v83, v83
	v_cvt_pk_f16_f32 v213, v214, v215
	v_mfma_f32_32x32x16_f16 v[64:79], v[184:187], v[152:155], v[64:79]
	ds_write_b64 v227, v[208:209] offset:9216
	ds_write_b64 v227, v[212:213] offset:13824
	ds_read_b128 v[184:187], v225 offset:64
	v_cvt_pk_f16_f32 v161, v82, v83
	v_add_f32_e32 v82, v82, v83
	v_exp_f32_e32 v84, v84
	v_exp_f32_e32 v85, v85
	v_mfma_f32_32x32x16_f16 v[64:79], v[188:191], v[156:159], v[64:79]
	ds_read_b128 v[188:191], v225 offset:96
	buffer_load_dwordx4 v[208:211], v229, s[4:7], s24 offen
	v_cvt_pk_f16_f32 v162, v84, v85
	v_add_f32_e32 v84, v84, v85
	v_add_f32_e32 v231, v80, v82
	v_exp_f32_e32 v86, v86
	v_exp_f32_e32 v87, v87
	s_waitcnt lgkmcnt(6)
	v_mfma_f32_32x32x16_f16 v[32:47], v[192:195], v[168:171], v[32:47]
	ds_read_b128 v[192:195], v226 offset:27648
	buffer_load_dwordx4 v[212:215], v252, s[4:7], s24 offen
	v_cvt_pk_f16_f32 v163, v86, v87
	v_add_f32_e32 v86, v86, v87
	v_add_f32_e32 v231, v231, v84
	v_exp_f32_e32 v88, v88
	v_exp_f32_e32 v89, v89
	v_mfma_f32_32x32x16_f16 v[48:63], v[196:199], v[168:171], v[48:63]
	ds_read_b128 v[196:199], v226 offset:32256
	v_cvt_pk_f16_f32 v164, v88, v89
	v_add_f32_e32 v88, v88, v89
	v_add_f32_e32 v231, v231, v86
	v_exp_f32_e32 v90, v90
	v_exp_f32_e32 v91, v91
	v_mfma_f32_32x32x16_f16 v[32:47], v[200:203], v[172:175], v[32:47]
	ds_read_b128 v[200:203], v226 offset:27680
	v_cvt_pk_f16_f32 v165, v90, v91
	v_add_f32_e32 v90, v90, v91
	v_add_f32_e32 v231, v231, v88
	v_exp_f32_e32 v92, v92
	v_exp_f32_e32 v93, v93
	v_mfma_f32_32x32x16_f16 v[48:63], v[204:207], v[172:175], v[48:63]
	ds_read_b128 v[204:207], v226 offset:32288
	v_cvt_pk_f16_f32 v166, v92, v93
	v_add_f32_e32 v92, v92, v93
	v_add_f32_e32 v231, v231, v90
	v_exp_f32_e32 v94, v94
	v_exp_f32_e32 v95, v95
	v_add_f32_e32 v231, v231, v92
	v_cvt_pk_f16_f32 v167, v94, v95
	v_add_f32_e32 v94, v94, v95
	v_add_f32_e32 v231, v231, v94
	v_cmp_nge_f32_e32 vcc, s34, v231
	s_cbranch_vccnz .Lovf_b1_30
.Lovfret_b1_30:
	v_add_f32_e32 v233, v233, v231
	s_waitcnt vmcnt(3)
	v_exp_f32_e32 v64, v64
	v_exp_f32_e32 v65, v65
	v_cvt_pk_f16_f32 v216, v216, v217
	v_cvt_pk_f16_f32 v217, v218, v219
	v_cvt_pk_f16_f32 v168, v64, v65
	v_add_f32_e32 v64, v64, v65
	v_cvt_pk_f16_f32 v218, v220, v221
	v_exp_f32_e32 v66, v66
	v_exp_f32_e32 v67, v67
	v_cvt_pk_f16_f32 v219, v222, v223
	ds_write_b128 v228, v[216:219] offset:0
	v_cvt_pk_f16_f32 v169, v66, v67
	v_add_f32_e32 v66, v66, v67
	v_exp_f32_e32 v68, v68
	v_exp_f32_e32 v69, v69
	buffer_load_dword v216, v230, s[4:7], s25 offen
	buffer_load_dword v217, v245, s[4:7], s25 offen
	v_cvt_pk_f16_f32 v170, v68, v69
	v_add_f32_e32 v68, v68, v69
	v_add_f32_e32 v231, v64, v66
	v_exp_f32_e32 v70, v70
	v_exp_f32_e32 v71, v71
	s_waitcnt lgkmcnt(1)
	v_mfma_f32_32x32x16_f16 v[32:47], v[192:195], v[160:163], v[32:47]
	ds_read_b128 v[192:195], v226 offset:27712
	buffer_load_dword v218, v246, s[4:7], s25 offen
	buffer_load_dword v219, v247, s[4:7], s25 offen
	v_cvt_pk_f16_f32 v171, v70, v71
	v_add_f32_e32 v70, v70, v71
	v_add_f32_e32 v231, v231, v68
	v_exp_f32_e32 v72, v72
	v_exp_f32_e32 v73, v73
	v_mfma_f32_32x32x16_f16 v[48:63], v[196:199], v[160:163], v[48:63]
	ds_read_b128 v[196:199], v226 offset:32320
	buffer_load_dword v220, v248, s[4:7], s25 offen
	buffer_load_dword v221, v249, s[4:7], s25 offen
	v_cvt_pk_f16_f32 v172, v72, v73
	v_add_f32_e32 v72, v72, v73
	v_add_f32_e32 v231, v231, v70
	v_exp_f32_e32 v74, v74
	v_exp_f32_e32 v75, v75
	v_mfma_f32_32x32x16_f16 v[32:47], v[200:203], v[164:167], v[32:47]
	ds_read_b128 v[200:203], v226 offset:27744
	buffer_load_dword v222, v250, s[4:7], s25 offen
	v_cvt_pk_f16_f32 v173, v74, v75
	v_add_f32_e32 v74, v74, v75
	v_add_f32_e32 v231, v231, v72
	v_exp_f32_e32 v76, v76
	v_exp_f32_e32 v77, v77
	v_mfma_f32_32x32x16_f16 v[48:63], v[204:207], v[164:167], v[48:63]
	ds_read_b128 v[204:207], v226 offset:32352
	buffer_load_dword v223, v251, s[4:7], s25 offen
	v_cvt_pk_f16_f32 v174, v76, v77
	v_add_f32_e32 v76, v76, v77
	v_add_f32_e32 v231, v231, v74
	v_exp_f32_e32 v78, v78
	v_exp_f32_e32 v79, v79
	v_add_f32_e32 v231, v231, v76
	v_cvt_pk_f16_f32 v175, v78, v79
	v_add_f32_e32 v78, v78, v79
	v_add_f32_e32 v231, v231, v78
	v_cmp_nge_f32_e32 vcc, s34, v231
	s_cbranch_vccnz .Lovf_b1_31
